# v55 + P7/P15 epilogue: power-of-two output scale folded into the fma (bias quads pre-scaled once per unit), 64 pk_mul per wave-unit removed; bit-identical
# speedup vs baseline: 1.0026x; 1.0026x over previous
.LBB0_662:
	s_add_u32 s12, s6, 0x23c00000
	s_mov_b64 s[14:15], 0x80
	s_addc_u32 s13, s7, 0
	s_add_i32 m0, s59, 0x18000
	v_lshl_add_u64 v[2:3], v[2:3], 0, s[14:15]
	s_and_b32 s22, s18, 3
	s_waitcnt vmcnt(2)
	s_barrier
	global_load_lds_dwordx4 v[2:3], off
	s_add_i32 m0, s59, 0x1a000
	s_add_u32 s16, s6, 0x12c00080
	v_lshl_add_u64 v[0:1], v[0:1], 0, s[14:15]
	s_addc_u32 s17, s7, 0
	s_add_i32 s63, s59, 0x8000
	s_add_i32 s64, s59, 0xa000
	global_load_lds_dwordx4 v[0:1], off
	v_lshl_add_u64 v[0:1], s[16:17], 0, v[164:165]
	s_mov_b32 m0, s63
	s_add_u32 s20, s34, 0x20080
	global_load_lds_dwordx4 v[0:1], off
	v_lshl_add_u64 v[0:1], s[16:17], 0, v[170:171]
	s_mov_b32 m0, s64
	s_addc_u32 s21, s35, 0
	global_load_lds_dwordx4 v[0:1], off
	s_add_i32 m0, s59, 0x1c000
	v_lshl_add_u64 v[0:1], s[20:21], 0, v[160:161]
	global_load_lds_dwordx4 v[0:1], off
	v_lshl_add_u64 v[0:1], s[20:21], 0, v[162:163]
	s_add_i32 m0, s59, 0x1e000
	v_lshrrev_b32_e32 v2, 2, v4
	global_load_lds_dwordx4 v[0:1], off
	v_lshrrev_b32_e32 v0, 1, v4
	v_lshrrev_b32_e32 v3, 3, v4
	s_cmp_lt_i32 s18, 4
	v_and_b32_e32 v0, 4, v0
	v_and_b32_e32 v1, 2, v4
	v_bitop3_b32 v2, v2, 1, v3 bitop3:0x48
	s_cselect_b64 s[18:19], -1, 0
	s_and_b32 s20, s2, 0x3fffffc0
	v_and_b32_e32 v171, 15, v4
	v_and_b32_e32 v204, 3, v5
	v_or3_b32 v0, v1, v0, v2
	s_add_i32 s67, 0, 0x20800
	s_lshl_b32 s20, s20, 2
	v_lshlrev_b32_e32 v1, 7, v171
	v_lshlrev_b32_e32 v3, 5, v204
	v_lshlrev_b32_e32 v0, 4, v0
	s_add_i32 s65, s67, s20
	v_lshl_or_b32 v2, s3, 13, v1
	v_xor_b32_e32 v0, v0, v3
	v_lshl_or_b32 v1, s22, 12, v1
	s_waitcnt vmcnt(6)
	s_cmpk_lt_u32 s2, 0x100
	v_or_b32_e32 v3, v2, v0
	v_or_b32_e32 v205, v1, v0
	v_bitop3_b32 v206, v1, 16, v0 bitop3:0x36
	v_bitop3_b32 v0, v2, 16, v0 bitop3:0x36
	s_cselect_b64 s[20:21], -1, 0
	s_lshl_b32 s2, s22, 7
	s_lshl_b32 s66, s22, 5
	s_add_i32 s67, s67, s2
	s_lshl_b32 s68, s3, 6
	s_add_i32 s69, 0, 0x10000
	s_add_i32 s70, 0, 0x10800
	s_add_i32 s71, 0, 0x14000
	s_add_i32 s72, 0, 0x14800
	v_add_u32_e32 v207, 0, v3
	v_add_u32_e32 v208, 0, v0
	v_mov_b32_e32 v209, 0x7f7f7f7f
	s_add_i32 s73, 0, 0x18800
	s_add_i32 s74, 0, 0x1c800
	s_mov_b32 s22, 0x3e000000
	s_mov_b32 s24, 0x42000000
	s_mov_b32 s75, 0xc3e00000
	v_mov_b32_e32 v210, 0x43e00000
	v_mov_b32_e32 v213, v164
	s_barrier
	s_branch .LBB0_665

.LBB0_677:
	v_mbcnt_lo_u32_b32 v250, -1, 0
	v_mbcnt_hi_u32_b32 v250, -1, v250
	v_bfe_u32 v250, v250, 4, 1
	v_mul_u32_u24_e32 v250, 0x78, v250
	v_mov_b32_e32 v251, 0
	s_lshl_b32 s27, s81, 10
	s_and_b32 s27, s27, 0x400
	v_mov_b32_e32 v17, v171
	v_mov_b32_e32 v16, v204
	s_add_i32 s27, s67, s27
	s_and_b64 vcc, exec, s[2:3]
	v_lshl_add_u32 v0, v16, 5, s27
	s_lshl_b32 s27, s80, 8
	s_or_b32 s27, s27, s66
	ds_read_b128 v[12:15], v0
	ds_read_b128 v[8:11], v0 offset:16
	ds_read_b128 v[4:7], v0 offset:512
	ds_read_b128 v[0:3], v0 offset:528
	v_lshl_add_u32 v16, v16, 3, s27
	s_lshl_b32 s27, s79, 8
	s_add_i32 s27, s27, s68
	v_add_u32_e32 v18, s27, v17
	s_waitcnt lgkmcnt(0)
	v_pk_mul_f32 v[0:1], v[0:1], s[24:25] op_sel_hi:[1,0]
	v_pk_mul_f32 v[2:3], v[2:3], s[24:25] op_sel_hi:[1,0]
	v_pk_mul_f32 v[4:5], v[4:5], s[24:25] op_sel_hi:[1,0]
	v_pk_mul_f32 v[6:7], v[6:7], s[24:25] op_sel_hi:[1,0]
	v_pk_mul_f32 v[8:9], v[8:9], s[24:25] op_sel_hi:[1,0]
	v_pk_mul_f32 v[10:11], v[10:11], s[24:25] op_sel_hi:[1,0]
	v_pk_mul_f32 v[12:13], v[12:13], s[24:25] op_sel_hi:[1,0]
	v_pk_mul_f32 v[14:15], v[14:15], s[24:25] op_sel_hi:[1,0]
	v_pk_fma_f32 v[22:23], v[158:159], s[22:23], v[14:15] op_sel_hi:[1,0,1]
	v_pk_fma_f32 v[24:25], v[156:157], s[22:23], v[12:13] op_sel_hi:[1,0,1]
	v_ashrrev_i32_e32 v19, 31, v18
	v_pk_fma_f32 v[28:29], v[152:153], s[22:23], v[8:9] op_sel_hi:[1,0,1]
	v_lshlrev_b64 v[20:21], 10, v[18:19]
	v_med3_f32 v19, v24, s75, v210
	v_med3_f32 v24, v25, s75, v210
	v_med3_f32 v25, v22, s75, v210
	v_med3_f32 v30, v23, s75, v210
	v_cvt_pk_fp8_f32 v22, v19, v24
	v_med3_f32 v19, v28, s75, v210
	v_med3_f32 v24, v29, s75, v210
	v_cvt_pk_fp8_f32 v23, v19, v24
	v_pk_fma_f32 v[26:27], v[154:155], s[22:23], v[10:11] op_sel_hi:[1,0,1]
	v_cvt_pk_fp8_f32 v22, v25, v30 op_sel:[0,0,1]
	v_pk_fma_f32 v[30:31], v[144:145], s[22:23], v[0:1] op_sel_hi:[1,0,1]
	v_med3_f32 v19, v26, s75, v210
	v_med3_f32 v24, v27, s75, v210
	v_cvt_pk_fp8_f32 v23, v19, v24 op_sel:[0,0,1]
	v_pk_fma_f32 v[24:25], v[150:151], s[22:23], v[6:7] op_sel_hi:[1,0,1]
	v_pk_fma_f32 v[26:27], v[148:149], s[22:23], v[4:5] op_sel_hi:[1,0,1]
	v_med3_f32 v19, v26, s75, v210
	v_med3_f32 v26, v27, s75, v210
	v_med3_f32 v27, v24, s75, v210
	v_med3_f32 v144, v25, s75, v210
	v_cvt_pk_fp8_f32 v24, v19, v26
	v_med3_f32 v19, v30, s75, v210
	v_med3_f32 v26, v31, s75, v210
	v_cvt_pk_fp8_f32 v25, v19, v26
	v_pk_fma_f32 v[28:29], v[146:147], s[22:23], v[2:3] op_sel_hi:[1,0,1]
	v_cvt_pk_fp8_f32 v24, v27, v144 op_sel:[0,0,1]
	v_ashrrev_i32_e32 v17, 31, v16
	v_med3_f32 v19, v28, s75, v210
	v_med3_f32 v26, v29, s75, v210
	v_cvt_pk_fp8_f32 v25, v19, v26 op_sel:[0,0,1]
	v_lshl_add_u64 v[20:21], s[12:13], 0, v[20:21]
	v_lshl_add_u64 v[20:21], v[20:21], 0, v[16:17]
	s_nop 1
	v_permlane16_swap_b32_e32 v22, v24
	v_permlane16_swap_b32_e32 v23, v25
	v_lshl_add_u64 v[248:249], v[20:21], 0, v[250:251]
	global_store_dwordx4 v[248:249], v[22:25], off
	s_nop 1
	v_pk_fma_f32 v[22:23], v[142:143], s[22:23], v[14:15] op_sel_hi:[1,0,1]
	v_pk_fma_f32 v[24:25], v[140:141], s[22:23], v[12:13] op_sel_hi:[1,0,1]
	v_pk_fma_f32 v[28:29], v[136:137], s[22:23], v[8:9] op_sel_hi:[1,0,1]
	v_med3_f32 v19, v24, s75, v210
	v_med3_f32 v24, v25, s75, v210
	v_med3_f32 v25, v22, s75, v210
	v_med3_f32 v30, v23, s75, v210
	v_cvt_pk_fp8_f32 v22, v19, v24
	v_med3_f32 v19, v28, s75, v210
	v_med3_f32 v24, v29, s75, v210
	v_cvt_pk_fp8_f32 v23, v19, v24
	v_pk_fma_f32 v[26:27], v[138:139], s[22:23], v[10:11] op_sel_hi:[1,0,1]
	v_cvt_pk_fp8_f32 v22, v25, v30 op_sel:[0,0,1]
	v_pk_fma_f32 v[30:31], v[128:129], s[22:23], v[0:1] op_sel_hi:[1,0,1]
	v_med3_f32 v19, v26, s75, v210
	v_med3_f32 v24, v27, s75, v210
	v_cvt_pk_fp8_f32 v23, v19, v24 op_sel:[0,0,1]
	v_pk_fma_f32 v[24:25], v[134:135], s[22:23], v[6:7] op_sel_hi:[1,0,1]
	v_pk_fma_f32 v[26:27], v[132:133], s[22:23], v[4:5] op_sel_hi:[1,0,1]
	v_med3_f32 v19, v26, s75, v210
	v_med3_f32 v26, v27, s75, v210
	v_med3_f32 v27, v24, s75, v210
	v_med3_f32 v128, v25, s75, v210
	v_cvt_pk_fp8_f32 v24, v19, v26
	v_med3_f32 v19, v30, s75, v210
	v_med3_f32 v26, v31, s75, v210
	v_cvt_pk_fp8_f32 v25, v19, v26
	v_pk_fma_f32 v[28:29], v[130:131], s[22:23], v[2:3] op_sel_hi:[1,0,1]
	v_add_u32_e32 v20, 16, v18
	v_ashrrev_i32_e32 v21, 31, v20
	v_med3_f32 v19, v28, s75, v210
	v_med3_f32 v26, v29, s75, v210
	v_lshlrev_b64 v[20:21], 10, v[20:21]
	v_cvt_pk_fp8_f32 v24, v27, v128 op_sel:[0,0,1]
	v_cvt_pk_fp8_f32 v25, v19, v26 op_sel:[0,0,1]
	v_lshl_add_u64 v[20:21], s[12:13], 0, v[20:21]
	v_lshl_add_u64 v[20:21], v[20:21], 0, v[16:17]
	s_nop 1
	v_permlane16_swap_b32_e32 v22, v24
	v_permlane16_swap_b32_e32 v23, v25
	v_lshl_add_u64 v[248:249], v[20:21], 0, v[250:251]
	global_store_dwordx4 v[248:249], v[22:25], off
	s_nop 1
	v_pk_fma_f32 v[22:23], v[126:127], s[22:23], v[14:15] op_sel_hi:[1,0,1]
	v_pk_fma_f32 v[24:25], v[124:125], s[22:23], v[12:13] op_sel_hi:[1,0,1]
	v_pk_fma_f32 v[28:29], v[120:121], s[22:23], v[8:9] op_sel_hi:[1,0,1]
	v_med3_f32 v19, v24, s75, v210
	v_med3_f32 v24, v25, s75, v210
	v_med3_f32 v25, v22, s75, v210
	v_med3_f32 v30, v23, s75, v210
	v_cvt_pk_fp8_f32 v22, v19, v24
	v_med3_f32 v19, v28, s75, v210
	v_med3_f32 v24, v29, s75, v210
	v_cvt_pk_fp8_f32 v23, v19, v24
	v_pk_fma_f32 v[26:27], v[122:123], s[22:23], v[10:11] op_sel_hi:[1,0,1]
	v_cvt_pk_fp8_f32 v22, v25, v30 op_sel:[0,0,1]
	v_pk_fma_f32 v[30:31], v[112:113], s[22:23], v[0:1] op_sel_hi:[1,0,1]
	v_med3_f32 v19, v26, s75, v210
	v_med3_f32 v24, v27, s75, v210
	v_cvt_pk_fp8_f32 v23, v19, v24 op_sel:[0,0,1]
	v_pk_fma_f32 v[24:25], v[118:119], s[22:23], v[6:7] op_sel_hi:[1,0,1]
	v_pk_fma_f32 v[26:27], v[116:117], s[22:23], v[4:5] op_sel_hi:[1,0,1]
	v_med3_f32 v19, v26, s75, v210
	v_med3_f32 v26, v27, s75, v210
	v_med3_f32 v27, v24, s75, v210
	v_med3_f32 v112, v25, s75, v210
	v_cvt_pk_fp8_f32 v24, v19, v26
	v_med3_f32 v19, v30, s75, v210
	v_med3_f32 v26, v31, s75, v210
	v_cvt_pk_fp8_f32 v25, v19, v26
	v_pk_fma_f32 v[28:29], v[114:115], s[22:23], v[2:3] op_sel_hi:[1,0,1]
	v_add_u32_e32 v20, 32, v18
	v_ashrrev_i32_e32 v21, 31, v20
	v_med3_f32 v19, v28, s75, v210
	v_med3_f32 v26, v29, s75, v210
	v_lshlrev_b64 v[20:21], 10, v[20:21]
	v_cvt_pk_fp8_f32 v24, v27, v112 op_sel:[0,0,1]
	v_cvt_pk_fp8_f32 v25, v19, v26 op_sel:[0,0,1]
	v_lshl_add_u64 v[20:21], s[12:13], 0, v[20:21]
	v_lshl_add_u64 v[20:21], v[20:21], 0, v[16:17]
	s_nop 1
	v_permlane16_swap_b32_e32 v22, v24
	v_permlane16_swap_b32_e32 v23, v25
	v_lshl_add_u64 v[248:249], v[20:21], 0, v[250:251]
	global_store_dwordx4 v[248:249], v[22:25], off
	s_nop 1
	v_pk_fma_f32 v[22:23], v[110:111], s[22:23], v[14:15] op_sel_hi:[1,0,1]
	v_pk_fma_f32 v[24:25], v[108:109], s[22:23], v[12:13] op_sel_hi:[1,0,1]
	v_pk_fma_f32 v[28:29], v[104:105], s[22:23], v[8:9] op_sel_hi:[1,0,1]
	v_med3_f32 v19, v24, s75, v210
	v_med3_f32 v24, v25, s75, v210
	v_med3_f32 v25, v22, s75, v210
	v_med3_f32 v30, v23, s75, v210
	v_cvt_pk_fp8_f32 v22, v19, v24
	v_med3_f32 v19, v28, s75, v210
	v_med3_f32 v24, v29, s75, v210
	v_cvt_pk_fp8_f32 v23, v19, v24
	v_pk_fma_f32 v[26:27], v[106:107], s[22:23], v[10:11] op_sel_hi:[1,0,1]
	v_cvt_pk_fp8_f32 v22, v25, v30 op_sel:[0,0,1]
	v_pk_fma_f32 v[30:31], v[96:97], s[22:23], v[0:1] op_sel_hi:[1,0,1]
	v_med3_f32 v19, v26, s75, v210
	v_med3_f32 v24, v27, s75, v210
	v_cvt_pk_fp8_f32 v23, v19, v24 op_sel:[0,0,1]
	v_pk_fma_f32 v[24:25], v[102:103], s[22:23], v[6:7] op_sel_hi:[1,0,1]
	v_pk_fma_f32 v[26:27], v[100:101], s[22:23], v[4:5] op_sel_hi:[1,0,1]
	v_med3_f32 v19, v26, s75, v210
	v_med3_f32 v26, v27, s75, v210
	v_med3_f32 v27, v24, s75, v210
	v_med3_f32 v96, v25, s75, v210
	v_cvt_pk_fp8_f32 v24, v19, v26
	v_med3_f32 v19, v30, s75, v210
	v_med3_f32 v26, v31, s75, v210
	v_cvt_pk_fp8_f32 v25, v19, v26
	v_pk_fma_f32 v[28:29], v[98:99], s[22:23], v[2:3] op_sel_hi:[1,0,1]
	v_add_u32_e32 v20, 48, v18
	v_ashrrev_i32_e32 v21, 31, v20
	v_med3_f32 v19, v28, s75, v210
	v_med3_f32 v26, v29, s75, v210
	v_lshlrev_b64 v[20:21], 10, v[20:21]
	v_cvt_pk_fp8_f32 v24, v27, v96 op_sel:[0,0,1]
	v_cvt_pk_fp8_f32 v25, v19, v26 op_sel:[0,0,1]
	v_lshl_add_u64 v[20:21], s[12:13], 0, v[20:21]
	v_lshl_add_u64 v[20:21], v[20:21], 0, v[16:17]
	s_nop 1
	v_permlane16_swap_b32_e32 v22, v24
	v_permlane16_swap_b32_e32 v23, v25
	v_lshl_add_u64 v[248:249], v[20:21], 0, v[250:251]
	global_store_dwordx4 v[248:249], v[22:25], off
	s_nop 1
	v_pk_fma_f32 v[22:23], v[94:95], s[22:23], v[14:15] op_sel_hi:[1,0,1]
	v_pk_fma_f32 v[24:25], v[92:93], s[22:23], v[12:13] op_sel_hi:[1,0,1]
	v_pk_fma_f32 v[28:29], v[88:89], s[22:23], v[8:9] op_sel_hi:[1,0,1]
	v_med3_f32 v19, v24, s75, v210
	v_med3_f32 v24, v25, s75, v210
	v_med3_f32 v25, v22, s75, v210
	v_med3_f32 v30, v23, s75, v210
	v_cvt_pk_fp8_f32 v22, v19, v24
	v_med3_f32 v19, v28, s75, v210
	v_med3_f32 v24, v29, s75, v210
	v_cvt_pk_fp8_f32 v23, v19, v24
	v_pk_fma_f32 v[26:27], v[90:91], s[22:23], v[10:11] op_sel_hi:[1,0,1]
	v_cvt_pk_fp8_f32 v22, v25, v30 op_sel:[0,0,1]
	v_pk_fma_f32 v[30:31], v[80:81], s[22:23], v[0:1] op_sel_hi:[1,0,1]
	v_med3_f32 v19, v26, s75, v210
	v_med3_f32 v24, v27, s75, v210
	v_cvt_pk_fp8_f32 v23, v19, v24 op_sel:[0,0,1]
	v_pk_fma_f32 v[24:25], v[86:87], s[22:23], v[6:7] op_sel_hi:[1,0,1]
	v_pk_fma_f32 v[26:27], v[84:85], s[22:23], v[4:5] op_sel_hi:[1,0,1]
	v_med3_f32 v19, v26, s75, v210
	v_med3_f32 v26, v27, s75, v210
	v_med3_f32 v27, v24, s75, v210
	v_med3_f32 v80, v25, s75, v210
	v_cvt_pk_fp8_f32 v24, v19, v26
	v_med3_f32 v19, v30, s75, v210
	v_med3_f32 v26, v31, s75, v210
	v_cvt_pk_fp8_f32 v25, v19, v26
	v_pk_fma_f32 v[28:29], v[82:83], s[22:23], v[2:3] op_sel_hi:[1,0,1]
	v_add_u32_e32 v20, 0x80, v18
	v_ashrrev_i32_e32 v21, 31, v20
	v_med3_f32 v19, v28, s75, v210
	v_med3_f32 v26, v29, s75, v210
	v_lshlrev_b64 v[20:21], 10, v[20:21]
	v_cvt_pk_fp8_f32 v24, v27, v80 op_sel:[0,0,1]
	v_cvt_pk_fp8_f32 v25, v19, v26 op_sel:[0,0,1]
	v_lshl_add_u64 v[20:21], s[12:13], 0, v[20:21]
	v_lshl_add_u64 v[20:21], v[20:21], 0, v[16:17]
	s_nop 1
	v_permlane16_swap_b32_e32 v22, v24
	v_permlane16_swap_b32_e32 v23, v25
	v_lshl_add_u64 v[248:249], v[20:21], 0, v[250:251]
	global_store_dwordx4 v[248:249], v[22:25], off
	s_nop 1
	v_pk_fma_f32 v[22:23], v[78:79], s[22:23], v[14:15] op_sel_hi:[1,0,1]
	v_pk_fma_f32 v[24:25], v[76:77], s[22:23], v[12:13] op_sel_hi:[1,0,1]
	v_pk_fma_f32 v[28:29], v[72:73], s[22:23], v[8:9] op_sel_hi:[1,0,1]
	v_med3_f32 v19, v24, s75, v210
	v_med3_f32 v24, v25, s75, v210
	v_med3_f32 v25, v22, s75, v210
	v_med3_f32 v30, v23, s75, v210
	v_cvt_pk_fp8_f32 v22, v19, v24
	v_med3_f32 v19, v28, s75, v210
	v_med3_f32 v24, v29, s75, v210
	v_cvt_pk_fp8_f32 v23, v19, v24
	v_pk_fma_f32 v[26:27], v[74:75], s[22:23], v[10:11] op_sel_hi:[1,0,1]
	v_cvt_pk_fp8_f32 v22, v25, v30 op_sel:[0,0,1]
	v_pk_fma_f32 v[30:31], v[64:65], s[22:23], v[0:1] op_sel_hi:[1,0,1]
	v_med3_f32 v19, v26, s75, v210
	v_med3_f32 v24, v27, s75, v210
	v_cvt_pk_fp8_f32 v23, v19, v24 op_sel:[0,0,1]
	v_pk_fma_f32 v[24:25], v[70:71], s[22:23], v[6:7] op_sel_hi:[1,0,1]
	v_pk_fma_f32 v[26:27], v[68:69], s[22:23], v[4:5] op_sel_hi:[1,0,1]
	v_med3_f32 v19, v26, s75, v210
	v_med3_f32 v26, v27, s75, v210
	v_med3_f32 v27, v24, s75, v210
	v_med3_f32 v64, v25, s75, v210
	v_cvt_pk_fp8_f32 v24, v19, v26
	v_med3_f32 v19, v30, s75, v210
	v_med3_f32 v26, v31, s75, v210
	v_cvt_pk_fp8_f32 v25, v19, v26
	v_pk_fma_f32 v[28:29], v[66:67], s[22:23], v[2:3] op_sel_hi:[1,0,1]
	v_add_u32_e32 v20, 0x90, v18
	v_ashrrev_i32_e32 v21, 31, v20
	v_med3_f32 v19, v28, s75, v210
	v_med3_f32 v26, v29, s75, v210
	v_lshlrev_b64 v[20:21], 10, v[20:21]
	v_cvt_pk_fp8_f32 v24, v27, v64 op_sel:[0,0,1]
	v_cvt_pk_fp8_f32 v25, v19, v26 op_sel:[0,0,1]
	v_lshl_add_u64 v[20:21], s[12:13], 0, v[20:21]
	v_lshl_add_u64 v[20:21], v[20:21], 0, v[16:17]
	s_nop 1
	v_permlane16_swap_b32_e32 v22, v24
	v_permlane16_swap_b32_e32 v23, v25
	v_lshl_add_u64 v[248:249], v[20:21], 0, v[250:251]
	global_store_dwordx4 v[248:249], v[22:25], off
	s_nop 1
	v_pk_fma_f32 v[22:23], v[62:63], s[22:23], v[14:15] op_sel_hi:[1,0,1]
	v_pk_fma_f32 v[24:25], v[60:61], s[22:23], v[12:13] op_sel_hi:[1,0,1]
	v_pk_fma_f32 v[28:29], v[56:57], s[22:23], v[8:9] op_sel_hi:[1,0,1]
	v_med3_f32 v19, v24, s75, v210
	v_med3_f32 v24, v25, s75, v210
	v_med3_f32 v25, v22, s75, v210
	v_med3_f32 v30, v23, s75, v210
	v_cvt_pk_fp8_f32 v22, v19, v24
	v_med3_f32 v19, v28, s75, v210
	v_med3_f32 v24, v29, s75, v210
	v_cvt_pk_fp8_f32 v23, v19, v24
	v_pk_fma_f32 v[26:27], v[58:59], s[22:23], v[10:11] op_sel_hi:[1,0,1]
	v_cvt_pk_fp8_f32 v22, v25, v30 op_sel:[0,0,1]
	v_pk_fma_f32 v[30:31], v[48:49], s[22:23], v[0:1] op_sel_hi:[1,0,1]
	v_med3_f32 v19, v26, s75, v210
	v_med3_f32 v24, v27, s75, v210
	v_cvt_pk_fp8_f32 v23, v19, v24 op_sel:[0,0,1]
	v_pk_fma_f32 v[24:25], v[54:55], s[22:23], v[6:7] op_sel_hi:[1,0,1]
	v_pk_fma_f32 v[26:27], v[52:53], s[22:23], v[4:5] op_sel_hi:[1,0,1]
	v_med3_f32 v19, v26, s75, v210
	v_med3_f32 v26, v27, s75, v210
	v_med3_f32 v27, v24, s75, v210
	v_med3_f32 v48, v25, s75, v210
	v_cvt_pk_fp8_f32 v24, v19, v26
	v_med3_f32 v19, v30, s75, v210
	v_med3_f32 v26, v31, s75, v210
	v_cvt_pk_fp8_f32 v25, v19, v26
	v_pk_fma_f32 v[28:29], v[50:51], s[22:23], v[2:3] op_sel_hi:[1,0,1]
	v_add_u32_e32 v20, 0xa0, v18
	v_ashrrev_i32_e32 v21, 31, v20
	v_med3_f32 v19, v28, s75, v210
	v_med3_f32 v26, v29, s75, v210
	v_lshlrev_b64 v[20:21], 10, v[20:21]
	v_cvt_pk_fp8_f32 v24, v27, v48 op_sel:[0,0,1]
	v_cvt_pk_fp8_f32 v25, v19, v26 op_sel:[0,0,1]
	v_lshl_add_u64 v[20:21], s[12:13], 0, v[20:21]
	v_pk_fma_f32 v[12:13], v[44:45], s[22:23], v[12:13] op_sel_hi:[1,0,1]
	v_lshl_add_u64 v[20:21], v[20:21], 0, v[16:17]
	v_pk_fma_f32 v[8:9], v[40:41], s[22:23], v[8:9] op_sel_hi:[1,0,1]
	s_nop 1
	v_permlane16_swap_b32_e32 v22, v24
	v_permlane16_swap_b32_e32 v23, v25
	v_lshl_add_u64 v[248:249], v[20:21], 0, v[250:251]
	global_store_dwordx4 v[248:249], v[22:25], off
	s_nop 1
	v_med3_f32 v20, v12, s75, v210
	v_med3_f32 v13, v13, s75, v210
	v_cvt_pk_fp8_f32 v12, v20, v13
	v_med3_f32 v8, v8, s75, v210
	v_med3_f32 v9, v9, s75, v210
	v_cvt_pk_fp8_f32 v13, v8, v9
	v_pk_fma_f32 v[10:11], v[42:43], s[22:23], v[10:11] op_sel_hi:[1,0,1]
	v_pk_fma_f32 v[4:5], v[36:37], s[22:23], v[4:5] op_sel_hi:[1,0,1]
	v_med3_f32 v8, v10, s75, v210
	v_med3_f32 v9, v11, s75, v210
	v_pk_fma_f32 v[0:1], v[32:33], s[22:23], v[0:1] op_sel_hi:[1,0,1]
	v_cvt_pk_fp8_f32 v13, v8, v9 op_sel:[0,0,1]
	v_med3_f32 v8, v4, s75, v210
	v_med3_f32 v5, v5, s75, v210
	v_cvt_pk_fp8_f32 v4, v8, v5
	v_med3_f32 v0, v0, s75, v210
	v_med3_f32 v1, v1, s75, v210
	v_pk_fma_f32 v[14:15], v[46:47], s[22:23], v[14:15] op_sel_hi:[1,0,1]
	v_cvt_pk_fp8_f32 v5, v0, v1
	v_pk_fma_f32 v[6:7], v[38:39], s[22:23], v[6:7] op_sel_hi:[1,0,1]
	v_pk_fma_f32 v[2:3], v[34:35], s[22:23], v[2:3] op_sel_hi:[1,0,1]
	v_add_u32_e32 v18, 0xb0, v18
	v_med3_f32 v14, v14, s75, v210
	v_med3_f32 v15, v15, s75, v210
	v_ashrrev_i32_e32 v19, 31, v18
	v_cvt_pk_fp8_f32 v12, v14, v15 op_sel:[0,0,1]
	v_med3_f32 v6, v6, s75, v210
	v_med3_f32 v7, v7, s75, v210
	v_med3_f32 v0, v2, s75, v210
	v_med3_f32 v1, v3, s75, v210
	v_lshlrev_b64 v[18:19], 10, v[18:19]
	v_cvt_pk_fp8_f32 v4, v6, v7 op_sel:[0,0,1]
	v_cvt_pk_fp8_f32 v5, v0, v1 op_sel:[0,0,1]
	v_lshl_add_u64 v[0:1], s[12:13], 0, v[18:19]
	v_lshl_add_u64 v[0:1], v[0:1], 0, v[16:17]
	s_mov_b64 s[2:3], -1
	global_store_dwordx2 v[0:1], v[12:13], off
	global_store_dwordx2 v[0:1], v[4:5], off offset:128
	s_cbranch_vccnz .LBB0_664
	s_andn2_b64 vcc, exec, s[10:11]
	s_cbranch_vccnz .LBB0_663
	s_barrier
	s_branch .LBB0_663

.LBB0_1796:
	s_lshl_b32 s27, s81, 10
	s_and_b32 s27, s27, 0x400
	v_mov_b32_e32 v17, v171
	v_mov_b32_e32 v16, v204
	s_add_i32 s27, s67, s27
	s_and_b64 vcc, exec, s[2:3]
	v_lshl_add_u32 v0, v16, 5, s27
	s_lshl_b32 s27, s80, 8
	s_or_b32 s27, s27, s66
	ds_read_b128 v[12:15], v0
	ds_read_b128 v[8:11], v0 offset:16
	ds_read_b128 v[4:7], v0 offset:512
	ds_read_b128 v[0:3], v0 offset:528
	v_lshl_add_u32 v16, v16, 3, s27
	s_lshl_b32 s27, s79, 8
	s_add_i32 s27, s27, s68
	v_add_u32_e32 v18, s27, v17
	s_waitcnt lgkmcnt(0)
	v_pk_mul_f32 v[0:1], v[0:1], s[24:25] op_sel_hi:[1,0]
	v_pk_mul_f32 v[2:3], v[2:3], s[24:25] op_sel_hi:[1,0]
	v_pk_mul_f32 v[4:5], v[4:5], s[24:25] op_sel_hi:[1,0]
	v_pk_mul_f32 v[6:7], v[6:7], s[24:25] op_sel_hi:[1,0]
	v_pk_mul_f32 v[8:9], v[8:9], s[24:25] op_sel_hi:[1,0]
	v_pk_mul_f32 v[10:11], v[10:11], s[24:25] op_sel_hi:[1,0]
	v_pk_mul_f32 v[12:13], v[12:13], s[24:25] op_sel_hi:[1,0]
	v_pk_mul_f32 v[14:15], v[14:15], s[24:25] op_sel_hi:[1,0]
	v_pk_fma_f32 v[22:23], v[158:159], s[22:23], v[14:15] op_sel_hi:[1,0,1]
	v_pk_fma_f32 v[24:25], v[156:157], s[22:23], v[12:13] op_sel_hi:[1,0,1]
	v_ashrrev_i32_e32 v19, 31, v18
	v_pk_fma_f32 v[28:29], v[152:153], s[22:23], v[8:9] op_sel_hi:[1,0,1]
	v_lshlrev_b64 v[20:21], 10, v[18:19]
	v_med3_f32 v19, v24, s75, v210
	v_med3_f32 v24, v25, s75, v210
	v_med3_f32 v25, v22, s75, v210
	v_med3_f32 v30, v23, s75, v210
	v_cvt_pk_fp8_f32 v22, v19, v24
	v_med3_f32 v19, v28, s75, v210
	v_med3_f32 v24, v29, s75, v210
	v_cvt_pk_fp8_f32 v23, v19, v24
	v_pk_fma_f32 v[26:27], v[154:155], s[22:23], v[10:11] op_sel_hi:[1,0,1]
	v_cvt_pk_fp8_f32 v22, v25, v30 op_sel:[0,0,1]
	v_pk_fma_f32 v[30:31], v[144:145], s[22:23], v[0:1] op_sel_hi:[1,0,1]
	v_med3_f32 v19, v26, s75, v210
	v_med3_f32 v24, v27, s75, v210
	v_cvt_pk_fp8_f32 v23, v19, v24 op_sel:[0,0,1]
	v_pk_fma_f32 v[24:25], v[150:151], s[22:23], v[6:7] op_sel_hi:[1,0,1]
	v_pk_fma_f32 v[26:27], v[148:149], s[22:23], v[4:5] op_sel_hi:[1,0,1]
	v_med3_f32 v19, v26, s75, v210
	v_med3_f32 v26, v27, s75, v210
	v_med3_f32 v27, v24, s75, v210
	v_med3_f32 v144, v25, s75, v210
	v_cvt_pk_fp8_f32 v24, v19, v26
	v_med3_f32 v19, v30, s75, v210
	v_med3_f32 v26, v31, s75, v210
	v_cvt_pk_fp8_f32 v25, v19, v26
	v_pk_fma_f32 v[28:29], v[146:147], s[22:23], v[2:3] op_sel_hi:[1,0,1]
	v_cvt_pk_fp8_f32 v24, v27, v144 op_sel:[0,0,1]
	v_ashrrev_i32_e32 v17, 31, v16
	v_med3_f32 v19, v28, s75, v210
	v_med3_f32 v26, v29, s75, v210
	v_cvt_pk_fp8_f32 v25, v19, v26 op_sel:[0,0,1]
	v_lshl_add_u64 v[20:21], s[12:13], 0, v[20:21]
	v_lshl_add_u64 v[20:21], v[20:21], 0, v[16:17]
	s_nop 1
	v_permlane16_swap_b32_e32 v22, v24
	v_permlane16_swap_b32_e32 v23, v25
	v_lshl_add_u64 v[248:249], v[20:21], 0, v[250:251]
	global_store_dwordx4 v[248:249], v[22:25], off
	s_nop 1
	v_pk_fma_f32 v[22:23], v[142:143], s[22:23], v[14:15] op_sel_hi:[1,0,1]
	v_pk_fma_f32 v[24:25], v[140:141], s[22:23], v[12:13] op_sel_hi:[1,0,1]
	v_pk_fma_f32 v[28:29], v[136:137], s[22:23], v[8:9] op_sel_hi:[1,0,1]
	v_med3_f32 v19, v24, s75, v210
	v_med3_f32 v24, v25, s75, v210
	v_med3_f32 v25, v22, s75, v210
	v_med3_f32 v30, v23, s75, v210
	v_cvt_pk_fp8_f32 v22, v19, v24
	v_med3_f32 v19, v28, s75, v210
	v_med3_f32 v24, v29, s75, v210
	v_cvt_pk_fp8_f32 v23, v19, v24
	v_pk_fma_f32 v[26:27], v[138:139], s[22:23], v[10:11] op_sel_hi:[1,0,1]
	v_cvt_pk_fp8_f32 v22, v25, v30 op_sel:[0,0,1]
	v_pk_fma_f32 v[30:31], v[128:129], s[22:23], v[0:1] op_sel_hi:[1,0,1]
	v_med3_f32 v19, v26, s75, v210
	v_med3_f32 v24, v27, s75, v210
	v_cvt_pk_fp8_f32 v23, v19, v24 op_sel:[0,0,1]
	v_pk_fma_f32 v[24:25], v[134:135], s[22:23], v[6:7] op_sel_hi:[1,0,1]
	v_pk_fma_f32 v[26:27], v[132:133], s[22:23], v[4:5] op_sel_hi:[1,0,1]
	v_med3_f32 v19, v26, s75, v210
	v_med3_f32 v26, v27, s75, v210
	v_med3_f32 v27, v24, s75, v210
	v_med3_f32 v128, v25, s75, v210
	v_cvt_pk_fp8_f32 v24, v19, v26
	v_med3_f32 v19, v30, s75, v210
	v_med3_f32 v26, v31, s75, v210
	v_cvt_pk_fp8_f32 v25, v19, v26
	v_pk_fma_f32 v[28:29], v[130:131], s[22:23], v[2:3] op_sel_hi:[1,0,1]
	v_add_u32_e32 v20, 16, v18
	v_ashrrev_i32_e32 v21, 31, v20
	v_med3_f32 v19, v28, s75, v210
	v_med3_f32 v26, v29, s75, v210
	v_lshlrev_b64 v[20:21], 10, v[20:21]
	v_cvt_pk_fp8_f32 v24, v27, v128 op_sel:[0,0,1]
	v_cvt_pk_fp8_f32 v25, v19, v26 op_sel:[0,0,1]
	v_lshl_add_u64 v[20:21], s[12:13], 0, v[20:21]
	v_lshl_add_u64 v[20:21], v[20:21], 0, v[16:17]
	s_nop 1
	v_permlane16_swap_b32_e32 v22, v24
	v_permlane16_swap_b32_e32 v23, v25
	v_lshl_add_u64 v[248:249], v[20:21], 0, v[250:251]
	global_store_dwordx4 v[248:249], v[22:25], off
	s_nop 1
	v_pk_fma_f32 v[22:23], v[126:127], s[22:23], v[14:15] op_sel_hi:[1,0,1]
	v_pk_fma_f32 v[24:25], v[124:125], s[22:23], v[12:13] op_sel_hi:[1,0,1]
	v_pk_fma_f32 v[28:29], v[120:121], s[22:23], v[8:9] op_sel_hi:[1,0,1]
	v_med3_f32 v19, v24, s75, v210
	v_med3_f32 v24, v25, s75, v210
	v_med3_f32 v25, v22, s75, v210
	v_med3_f32 v30, v23, s75, v210
	v_cvt_pk_fp8_f32 v22, v19, v24
	v_med3_f32 v19, v28, s75, v210
	v_med3_f32 v24, v29, s75, v210
	v_cvt_pk_fp8_f32 v23, v19, v24
	v_pk_fma_f32 v[26:27], v[122:123], s[22:23], v[10:11] op_sel_hi:[1,0,1]
	v_cvt_pk_fp8_f32 v22, v25, v30 op_sel:[0,0,1]
	v_pk_fma_f32 v[30:31], v[112:113], s[22:23], v[0:1] op_sel_hi:[1,0,1]
	v_med3_f32 v19, v26, s75, v210
	v_med3_f32 v24, v27, s75, v210
	v_cvt_pk_fp8_f32 v23, v19, v24 op_sel:[0,0,1]
	v_pk_fma_f32 v[24:25], v[118:119], s[22:23], v[6:7] op_sel_hi:[1,0,1]
	v_pk_fma_f32 v[26:27], v[116:117], s[22:23], v[4:5] op_sel_hi:[1,0,1]
	v_med3_f32 v19, v26, s75, v210
	v_med3_f32 v26, v27, s75, v210
	v_med3_f32 v27, v24, s75, v210
	v_med3_f32 v112, v25, s75, v210
	v_cvt_pk_fp8_f32 v24, v19, v26
	v_med3_f32 v19, v30, s75, v210
	v_med3_f32 v26, v31, s75, v210
	v_cvt_pk_fp8_f32 v25, v19, v26
	v_pk_fma_f32 v[28:29], v[114:115], s[22:23], v[2:3] op_sel_hi:[1,0,1]
	v_add_u32_e32 v20, 32, v18
	v_ashrrev_i32_e32 v21, 31, v20
	v_med3_f32 v19, v28, s75, v210
	v_med3_f32 v26, v29, s75, v210
	v_lshlrev_b64 v[20:21], 10, v[20:21]
	v_cvt_pk_fp8_f32 v24, v27, v112 op_sel:[0,0,1]
	v_cvt_pk_fp8_f32 v25, v19, v26 op_sel:[0,0,1]
	v_lshl_add_u64 v[20:21], s[12:13], 0, v[20:21]
	v_lshl_add_u64 v[20:21], v[20:21], 0, v[16:17]
	s_nop 1
	v_permlane16_swap_b32_e32 v22, v24
	v_permlane16_swap_b32_e32 v23, v25
	v_lshl_add_u64 v[248:249], v[20:21], 0, v[250:251]
	global_store_dwordx4 v[248:249], v[22:25], off
	s_nop 1
	v_pk_fma_f32 v[22:23], v[110:111], s[22:23], v[14:15] op_sel_hi:[1,0,1]
	v_pk_fma_f32 v[24:25], v[108:109], s[22:23], v[12:13] op_sel_hi:[1,0,1]
	v_pk_fma_f32 v[28:29], v[104:105], s[22:23], v[8:9] op_sel_hi:[1,0,1]
	v_med3_f32 v19, v24, s75, v210
	v_med3_f32 v24, v25, s75, v210
	v_med3_f32 v25, v22, s75, v210
	v_med3_f32 v30, v23, s75, v210
	v_cvt_pk_fp8_f32 v22, v19, v24
	v_med3_f32 v19, v28, s75, v210
	v_med3_f32 v24, v29, s75, v210
	v_cvt_pk_fp8_f32 v23, v19, v24
	v_pk_fma_f32 v[26:27], v[106:107], s[22:23], v[10:11] op_sel_hi:[1,0,1]
	v_cvt_pk_fp8_f32 v22, v25, v30 op_sel:[0,0,1]
	v_pk_fma_f32 v[30:31], v[96:97], s[22:23], v[0:1] op_sel_hi:[1,0,1]
	v_med3_f32 v19, v26, s75, v210
	v_med3_f32 v24, v27, s75, v210
	v_cvt_pk_fp8_f32 v23, v19, v24 op_sel:[0,0,1]
	v_pk_fma_f32 v[24:25], v[102:103], s[22:23], v[6:7] op_sel_hi:[1,0,1]
	v_pk_fma_f32 v[26:27], v[100:101], s[22:23], v[4:5] op_sel_hi:[1,0,1]
	v_med3_f32 v19, v26, s75, v210
	v_med3_f32 v26, v27, s75, v210
	v_med3_f32 v27, v24, s75, v210
	v_med3_f32 v96, v25, s75, v210
	v_cvt_pk_fp8_f32 v24, v19, v26
	v_med3_f32 v19, v30, s75, v210
	v_med3_f32 v26, v31, s75, v210
	v_cvt_pk_fp8_f32 v25, v19, v26
	v_pk_fma_f32 v[28:29], v[98:99], s[22:23], v[2:3] op_sel_hi:[1,0,1]
	v_add_u32_e32 v20, 48, v18
	v_ashrrev_i32_e32 v21, 31, v20
	v_med3_f32 v19, v28, s75, v210
	v_med3_f32 v26, v29, s75, v210
	v_lshlrev_b64 v[20:21], 10, v[20:21]
	v_cvt_pk_fp8_f32 v24, v27, v96 op_sel:[0,0,1]
	v_cvt_pk_fp8_f32 v25, v19, v26 op_sel:[0,0,1]
	v_lshl_add_u64 v[20:21], s[12:13], 0, v[20:21]
	v_lshl_add_u64 v[20:21], v[20:21], 0, v[16:17]
	s_nop 1
	v_permlane16_swap_b32_e32 v22, v24
	v_permlane16_swap_b32_e32 v23, v25
	v_lshl_add_u64 v[248:249], v[20:21], 0, v[250:251]
	global_store_dwordx4 v[248:249], v[22:25], off
	s_nop 1
	v_pk_fma_f32 v[22:23], v[94:95], s[22:23], v[14:15] op_sel_hi:[1,0,1]
	v_pk_fma_f32 v[24:25], v[92:93], s[22:23], v[12:13] op_sel_hi:[1,0,1]
	v_pk_fma_f32 v[28:29], v[88:89], s[22:23], v[8:9] op_sel_hi:[1,0,1]
	v_med3_f32 v19, v24, s75, v210
	v_med3_f32 v24, v25, s75, v210
	v_med3_f32 v25, v22, s75, v210
	v_med3_f32 v30, v23, s75, v210
	v_cvt_pk_fp8_f32 v22, v19, v24
	v_med3_f32 v19, v28, s75, v210
	v_med3_f32 v24, v29, s75, v210
	v_cvt_pk_fp8_f32 v23, v19, v24
	v_pk_fma_f32 v[26:27], v[90:91], s[22:23], v[10:11] op_sel_hi:[1,0,1]
	v_cvt_pk_fp8_f32 v22, v25, v30 op_sel:[0,0,1]
	v_pk_fma_f32 v[30:31], v[80:81], s[22:23], v[0:1] op_sel_hi:[1,0,1]
	v_med3_f32 v19, v26, s75, v210
	v_med3_f32 v24, v27, s75, v210
	v_cvt_pk_fp8_f32 v23, v19, v24 op_sel:[0,0,1]
	v_pk_fma_f32 v[24:25], v[86:87], s[22:23], v[6:7] op_sel_hi:[1,0,1]
	v_pk_fma_f32 v[26:27], v[84:85], s[22:23], v[4:5] op_sel_hi:[1,0,1]
	v_med3_f32 v19, v26, s75, v210
	v_med3_f32 v26, v27, s75, v210
	v_med3_f32 v27, v24, s75, v210
	v_med3_f32 v80, v25, s75, v210
	v_cvt_pk_fp8_f32 v24, v19, v26
	v_med3_f32 v19, v30, s75, v210
	v_med3_f32 v26, v31, s75, v210
	v_cvt_pk_fp8_f32 v25, v19, v26
	v_pk_fma_f32 v[28:29], v[82:83], s[22:23], v[2:3] op_sel_hi:[1,0,1]
	v_add_u32_e32 v20, 0x80, v18
	v_ashrrev_i32_e32 v21, 31, v20
	v_med3_f32 v19, v28, s75, v210
	v_med3_f32 v26, v29, s75, v210
	v_lshlrev_b64 v[20:21], 10, v[20:21]
	v_cvt_pk_fp8_f32 v24, v27, v80 op_sel:[0,0,1]
	v_cvt_pk_fp8_f32 v25, v19, v26 op_sel:[0,0,1]
	v_lshl_add_u64 v[20:21], s[12:13], 0, v[20:21]
	v_lshl_add_u64 v[20:21], v[20:21], 0, v[16:17]
	s_nop 1
	v_permlane16_swap_b32_e32 v22, v24
	v_permlane16_swap_b32_e32 v23, v25
	v_lshl_add_u64 v[248:249], v[20:21], 0, v[250:251]
	global_store_dwordx4 v[248:249], v[22:25], off
	s_nop 1
	v_pk_fma_f32 v[22:23], v[78:79], s[22:23], v[14:15] op_sel_hi:[1,0,1]
	v_pk_fma_f32 v[24:25], v[76:77], s[22:23], v[12:13] op_sel_hi:[1,0,1]
	v_pk_fma_f32 v[28:29], v[72:73], s[22:23], v[8:9] op_sel_hi:[1,0,1]
	v_med3_f32 v19, v24, s75, v210
	v_med3_f32 v24, v25, s75, v210
	v_med3_f32 v25, v22, s75, v210
	v_med3_f32 v30, v23, s75, v210
	v_cvt_pk_fp8_f32 v22, v19, v24
	v_med3_f32 v19, v28, s75, v210
	v_med3_f32 v24, v29, s75, v210
	v_cvt_pk_fp8_f32 v23, v19, v24
	v_pk_fma_f32 v[26:27], v[74:75], s[22:23], v[10:11] op_sel_hi:[1,0,1]
	v_cvt_pk_fp8_f32 v22, v25, v30 op_sel:[0,0,1]
	v_pk_fma_f32 v[30:31], v[64:65], s[22:23], v[0:1] op_sel_hi:[1,0,1]
	v_med3_f32 v19, v26, s75, v210
	v_med3_f32 v24, v27, s75, v210
	v_cvt_pk_fp8_f32 v23, v19, v24 op_sel:[0,0,1]
	v_pk_fma_f32 v[24:25], v[70:71], s[22:23], v[6:7] op_sel_hi:[1,0,1]
	v_pk_fma_f32 v[26:27], v[68:69], s[22:23], v[4:5] op_sel_hi:[1,0,1]
	v_med3_f32 v19, v26, s75, v210
	v_med3_f32 v26, v27, s75, v210
	v_med3_f32 v27, v24, s75, v210
	v_med3_f32 v64, v25, s75, v210
	v_cvt_pk_fp8_f32 v24, v19, v26
	v_med3_f32 v19, v30, s75, v210
	v_med3_f32 v26, v31, s75, v210
	v_cvt_pk_fp8_f32 v25, v19, v26
	v_pk_fma_f32 v[28:29], v[66:67], s[22:23], v[2:3] op_sel_hi:[1,0,1]
	v_add_u32_e32 v20, 0x90, v18
	v_ashrrev_i32_e32 v21, 31, v20
	v_med3_f32 v19, v28, s75, v210
	v_med3_f32 v26, v29, s75, v210
	v_lshlrev_b64 v[20:21], 10, v[20:21]
	v_cvt_pk_fp8_f32 v24, v27, v64 op_sel:[0,0,1]
	v_cvt_pk_fp8_f32 v25, v19, v26 op_sel:[0,0,1]
	v_lshl_add_u64 v[20:21], s[12:13], 0, v[20:21]
	v_lshl_add_u64 v[20:21], v[20:21], 0, v[16:17]
	s_nop 1
	v_permlane16_swap_b32_e32 v22, v24
	v_permlane16_swap_b32_e32 v23, v25
	v_lshl_add_u64 v[248:249], v[20:21], 0, v[250:251]
	global_store_dwordx4 v[248:249], v[22:25], off
	s_nop 1
	v_pk_fma_f32 v[22:23], v[62:63], s[22:23], v[14:15] op_sel_hi:[1,0,1]
	v_pk_fma_f32 v[24:25], v[60:61], s[22:23], v[12:13] op_sel_hi:[1,0,1]
	v_pk_fma_f32 v[28:29], v[56:57], s[22:23], v[8:9] op_sel_hi:[1,0,1]
	v_med3_f32 v19, v24, s75, v210
	v_med3_f32 v24, v25, s75, v210
	v_med3_f32 v25, v22, s75, v210
	v_med3_f32 v30, v23, s75, v210
	v_cvt_pk_fp8_f32 v22, v19, v24
	v_med3_f32 v19, v28, s75, v210
	v_med3_f32 v24, v29, s75, v210
	v_cvt_pk_fp8_f32 v23, v19, v24
	v_pk_fma_f32 v[26:27], v[58:59], s[22:23], v[10:11] op_sel_hi:[1,0,1]
	v_cvt_pk_fp8_f32 v22, v25, v30 op_sel:[0,0,1]
	v_pk_fma_f32 v[30:31], v[48:49], s[22:23], v[0:1] op_sel_hi:[1,0,1]
	v_med3_f32 v19, v26, s75, v210
	v_med3_f32 v24, v27, s75, v210
	v_cvt_pk_fp8_f32 v23, v19, v24 op_sel:[0,0,1]
	v_pk_fma_f32 v[24:25], v[54:55], s[22:23], v[6:7] op_sel_hi:[1,0,1]
	v_pk_fma_f32 v[26:27], v[52:53], s[22:23], v[4:5] op_sel_hi:[1,0,1]
	v_med3_f32 v19, v26, s75, v210
	v_med3_f32 v26, v27, s75, v210
	v_med3_f32 v27, v24, s75, v210
	v_med3_f32 v48, v25, s75, v210
	v_cvt_pk_fp8_f32 v24, v19, v26
	v_med3_f32 v19, v30, s75, v210
	v_med3_f32 v26, v31, s75, v210
	v_cvt_pk_fp8_f32 v25, v19, v26
	v_pk_fma_f32 v[28:29], v[50:51], s[22:23], v[2:3] op_sel_hi:[1,0,1]
	v_add_u32_e32 v20, 0xa0, v18
	v_ashrrev_i32_e32 v21, 31, v20
	v_med3_f32 v19, v28, s75, v210
	v_med3_f32 v26, v29, s75, v210
	v_lshlrev_b64 v[20:21], 10, v[20:21]
	v_cvt_pk_fp8_f32 v24, v27, v48 op_sel:[0,0,1]
	v_cvt_pk_fp8_f32 v25, v19, v26 op_sel:[0,0,1]
	v_lshl_add_u64 v[20:21], s[12:13], 0, v[20:21]
	v_pk_fma_f32 v[12:13], v[44:45], s[22:23], v[12:13] op_sel_hi:[1,0,1]
	v_lshl_add_u64 v[20:21], v[20:21], 0, v[16:17]
	v_pk_fma_f32 v[8:9], v[40:41], s[22:23], v[8:9] op_sel_hi:[1,0,1]
	s_nop 1
	v_permlane16_swap_b32_e32 v22, v24
	v_permlane16_swap_b32_e32 v23, v25
	v_lshl_add_u64 v[248:249], v[20:21], 0, v[250:251]
	global_store_dwordx4 v[248:249], v[22:25], off
	s_nop 1
	v_med3_f32 v20, v12, s75, v210
	v_med3_f32 v13, v13, s75, v210
	v_cvt_pk_fp8_f32 v12, v20, v13
	v_med3_f32 v8, v8, s75, v210
	v_med3_f32 v9, v9, s75, v210
	v_cvt_pk_fp8_f32 v13, v8, v9
	v_pk_fma_f32 v[10:11], v[42:43], s[22:23], v[10:11] op_sel_hi:[1,0,1]
	v_pk_fma_f32 v[4:5], v[36:37], s[22:23], v[4:5] op_sel_hi:[1,0,1]
	v_med3_f32 v8, v10, s75, v210
	v_med3_f32 v9, v11, s75, v210
	v_pk_fma_f32 v[0:1], v[32:33], s[22:23], v[0:1] op_sel_hi:[1,0,1]
	v_cvt_pk_fp8_f32 v13, v8, v9 op_sel:[0,0,1]
	v_med3_f32 v8, v4, s75, v210
	v_med3_f32 v5, v5, s75, v210
	v_cvt_pk_fp8_f32 v4, v8, v5
	v_med3_f32 v0, v0, s75, v210
	v_med3_f32 v1, v1, s75, v210
	v_pk_fma_f32 v[14:15], v[46:47], s[22:23], v[14:15] op_sel_hi:[1,0,1]
	v_cvt_pk_fp8_f32 v5, v0, v1
	v_pk_fma_f32 v[6:7], v[38:39], s[22:23], v[6:7] op_sel_hi:[1,0,1]
	v_pk_fma_f32 v[2:3], v[34:35], s[22:23], v[2:3] op_sel_hi:[1,0,1]
	v_add_u32_e32 v18, 0xb0, v18
	v_med3_f32 v14, v14, s75, v210
	v_med3_f32 v15, v15, s75, v210
	v_ashrrev_i32_e32 v19, 31, v18
	v_cvt_pk_fp8_f32 v12, v14, v15 op_sel:[0,0,1]
	v_med3_f32 v6, v6, s75, v210
	v_med3_f32 v7, v7, s75, v210
	v_med3_f32 v0, v2, s75, v210
	v_med3_f32 v1, v3, s75, v210
	v_lshlrev_b64 v[18:19], 10, v[18:19]
	v_cvt_pk_fp8_f32 v4, v6, v7 op_sel:[0,0,1]
	v_cvt_pk_fp8_f32 v5, v0, v1 op_sel:[0,0,1]
	v_lshl_add_u64 v[0:1], s[12:13], 0, v[18:19]
	v_lshl_add_u64 v[0:1], v[0:1], 0, v[16:17]
	s_mov_b64 s[2:3], -1
	global_store_dwordx2 v[0:1], v[12:13], off
	global_store_dwordx2 v[0:1], v[4:5], off offset:128
	s_cbranch_vccnz .LBB0_1783
	s_andn2_b64 vcc, exec, s[10:11]
	s_cbranch_vccnz .LBB0_1782
	s_barrier
	s_branch .LBB0_1782
